# speedup vs baseline: 1.0103x; 1.0009x over previous
.LBB2_1:
	v_mfma_f32_32x32x16_f16 v[96:111], v[172:175], v[136:139], v[0:15]
	s_mov_b32 s17, s31
	s_mov_b32 s18, s15
	v_add_u32_e32 v185, s18, v181
	ds_read_b64_tr_b16 v[176:177], v185 offset:24576
	ds_read_b64_tr_b16 v[178:179], v185 offset:25088
	v_add_f32_e32 v80, v64, v65
	v_add_f32_e32 v80, v66, v80
	v_add_f32_e32 v80, v67, v80
	v_add_f32_e32 v80, v68, v80
	v_add_f32_e32 v80, v69, v80
	v_cvt_pk_f16_f32 v140, v64, v65
	v_cvt_pk_f16_f32 v141, v66, v67
	ds_read_b64_tr_b16 v[172:173], v185 offset:28672
	ds_read_b64_tr_b16 v[174:175], v185 offset:29184
	v_add_f32_e32 v64, v70, v80
	s_waitcnt lgkmcnt(10)
	v_mfma_f32_32x32x16_f16 v[80:95], v[168:171], v[136:139], v[0:15]
	v_add_f32_e32 v64, v71, v64
	v_add_f32_e32 v64, v72, v64
	v_add_f32_e32 v64, v73, v64
	v_cvt_pk_f16_f32 v142, v68, v69
	v_cvt_pk_f16_f32 v143, v70, v71
	ds_read_b64_tr_b16 v[68:69], v185 offset:25600
	ds_read_b64_tr_b16 v[70:71], v185 offset:26112
	s_waitcnt lgkmcnt(11)
	v_mfma_f32_32x32x16_f16 v[96:111], v[164:167], v[128:131], v[96:111]
	v_add_f32_e32 v64, v74, v64
	v_add_f32_e32 v64, v75, v64
	v_add_f32_e32 v64, v76, v64
	v_add_f32_e32 v116, v77, v64
	v_cvt_pk_f16_f32 v132, v72, v73
	v_cvt_pk_f16_f32 v133, v74, v75
	ds_read_b64_tr_b16 v[64:65], v185 offset:29696
	ds_read_b64_tr_b16 v[66:67], v185 offset:30208
	s_waitcnt lgkmcnt(12)
	v_mfma_f32_32x32x16_f16 v[80:95], v[160:163], v[128:131], v[80:95]
	v_add_f32_e32 v72, v78, v116
	v_add_f32_e32 v72, v79, v72
	v_add_f32_e32 v72, v48, v72
	v_add_f32_e32 v116, v49, v72
	v_cvt_pk_f16_f32 v134, v76, v77
	v_cvt_pk_f16_f32 v135, v78, v79
	ds_read_b64_tr_b16 v[72:73], v185 offset:26624
	ds_read_b64_tr_b16 v[74:75], v185 offset:27136
	s_waitcnt lgkmcnt(13)
	v_mfma_f32_32x32x16_f16 v[96:111], v[156:159], v[120:123], v[96:111]
	v_add_f32_e32 v76, v50, v116
	v_add_f32_e32 v76, v51, v76
	v_add_f32_e32 v76, v52, v76
	v_add_f32_e32 v76, v53, v76
	v_cvt_pk_f16_f32 v124, v48, v49
	v_cvt_pk_f16_f32 v125, v50, v51
	ds_read_b64_tr_b16 v[48:49], v185 offset:30720
	ds_read_b64_tr_b16 v[50:51], v185 offset:31232
	s_waitcnt lgkmcnt(14)
	v_mfma_f32_32x32x16_f16 v[80:95], v[152:155], v[120:123], v[80:95]
	v_add_f32_e32 v76, v54, v76
	v_add_f32_e32 v76, v55, v76
	v_add_f32_e32 v76, v56, v76
	v_add_f32_e32 v76, v57, v76
	v_cvt_pk_f16_f32 v126, v52, v53
	v_cvt_pk_f16_f32 v127, v54, v55
	ds_read_b64_tr_b16 v[52:53], v185 offset:27648
	ds_read_b64_tr_b16 v[54:55], v185 offset:28160
	s_waitcnt lgkmcnt(14)
	v_mfma_f32_32x32x16_f16 v[96:111], v[148:151], v[112:115], v[96:111]
	v_add_f32_e32 v76, v58, v76
	v_add_f32_e32 v76, v59, v76
	v_add_f32_e32 v76, v60, v76
	v_add_f32_e32 v76, v61, v76
	v_cvt_pk_f16_f32 v116, v56, v57
	v_cvt_pk_f16_f32 v117, v58, v59
	ds_read_b64_tr_b16 v[56:57], v185 offset:31744
	ds_read_b64_tr_b16 v[58:59], v185 offset:32256
	v_mfma_f32_32x32x16_f16 v[80:95], v[144:147], v[112:115], v[80:95]
	v_add_f32_e32 v76, v62, v76
	v_add_f32_e32 v76, v63, v76
	v_cvt_pk_f16_f32 v118, v60, v61
	v_cvt_pk_f16_f32 v119, v62, v63
	s_add_i32 m0, s14, s25
	v_cmp_lt_f32_e32 vcc, s36, v76
	global_load_lds_dwordx4 v180, s[44:45]
	s_add_i32 m0, s28, s26
	s_add_u32 s44, s44, 0x2000
	global_load_lds_dwordx4 v180, s[46:47]
	s_addc_u32 s45, s45, 0
	s_add_u32 s46, s46, 0x2000
	s_addc_u32 s47, s47, 0
	s_cbranch_vccnz .Lmy_rare_1

.LBB2_4:
	v_mfma_f32_32x32x16_f16 v[64:79], v[60:63], v[136:139], v[0:15]
	v_add_u32_e32 v185, s17, v181
	ds_read_b64_tr_b16 v[144:145], v185 offset:24576
	ds_read_b64_tr_b16 v[146:147], v185 offset:25088
	v_add_f32_e32 v48, v96, v97
	v_add_f32_e32 v48, v98, v48
	v_add_f32_e32 v48, v99, v48
	v_add_f32_e32 v48, v100, v48
	v_add_f32_e32 v48, v101, v48
	v_cvt_pk_f16_f32 v140, v96, v97
	v_cvt_pk_f16_f32 v141, v98, v99
	ds_read_b64_tr_b16 v[152:153], v185 offset:28672
	ds_read_b64_tr_b16 v[154:155], v185 offset:29184
	v_add_f32_e32 v48, v102, v48
	v_add_f32_e32 v48, v103, v48
	v_add_f32_e32 v48, v104, v48
	v_add_f32_e32 v96, v105, v48
	s_waitcnt lgkmcnt(10)
	v_mfma_f32_32x32x16_f16 v[48:63], v[148:151], v[136:139], v[0:15]
	v_cvt_pk_f16_f32 v142, v100, v101
	v_cvt_pk_f16_f32 v143, v102, v103
	ds_read_b64_tr_b16 v[148:149], v185 offset:25600
	ds_read_b64_tr_b16 v[150:151], v185 offset:26112
	s_waitcnt lgkmcnt(11)
	v_mfma_f32_32x32x16_f16 v[64:79], v[176:179], v[128:131], v[64:79]
	v_add_f32_e32 v96, v106, v96
	v_add_f32_e32 v96, v107, v96
	v_add_f32_e32 v96, v108, v96
	v_add_f32_e32 v96, v109, v96
	v_cvt_pk_f16_f32 v132, v104, v105
	v_cvt_pk_f16_f32 v133, v106, v107
	ds_read_b64_tr_b16 v[100:101], v185 offset:29696
	ds_read_b64_tr_b16 v[102:103], v185 offset:30208
	s_waitcnt lgkmcnt(12)
	v_mfma_f32_32x32x16_f16 v[48:63], v[172:175], v[128:131], v[48:63]
	v_add_f32_e32 v96, v110, v96
	v_add_f32_e32 v96, v111, v96
	v_add_f32_e32 v96, v80, v96
	v_add_f32_e32 v104, v81, v96
	v_cvt_pk_f16_f32 v134, v108, v109
	v_cvt_pk_f16_f32 v135, v110, v111
	ds_read_b64_tr_b16 v[96:97], v185 offset:26624
	ds_read_b64_tr_b16 v[98:99], v185 offset:27136
	s_waitcnt lgkmcnt(13)
	v_mfma_f32_32x32x16_f16 v[64:79], v[168:171], v[120:123], v[64:79]
	v_add_f32_e32 v104, v82, v104
	v_add_f32_e32 v104, v83, v104
	v_add_f32_e32 v104, v84, v104
	v_add_f32_e32 v104, v85, v104
	v_cvt_pk_f16_f32 v124, v80, v81
	v_cvt_pk_f16_f32 v125, v82, v83
	ds_read_b64_tr_b16 v[80:81], v185 offset:30720
	ds_read_b64_tr_b16 v[82:83], v185 offset:31232
	s_waitcnt lgkmcnt(14)
	v_mfma_f32_32x32x16_f16 v[48:63], v[164:167], v[120:123], v[48:63]
	v_add_f32_e32 v104, v86, v104
	v_add_f32_e32 v104, v87, v104
	v_add_f32_e32 v104, v88, v104
	v_add_f32_e32 v104, v89, v104
	v_cvt_pk_f16_f32 v126, v84, v85
	v_cvt_pk_f16_f32 v127, v86, v87
	ds_read_b64_tr_b16 v[84:85], v185 offset:27648
	ds_read_b64_tr_b16 v[86:87], v185 offset:28160
	s_waitcnt lgkmcnt(14)
	v_mfma_f32_32x32x16_f16 v[64:79], v[160:163], v[112:115], v[64:79]
	v_add_f32_e32 v104, v90, v104
	v_add_f32_e32 v104, v91, v104
	v_add_f32_e32 v104, v92, v104
	v_add_f32_e32 v104, v93, v104
	v_cvt_pk_f16_f32 v116, v88, v89
	v_cvt_pk_f16_f32 v117, v90, v91
	ds_read_b64_tr_b16 v[88:89], v185 offset:31744
	ds_read_b64_tr_b16 v[90:91], v185 offset:32256
	v_mfma_f32_32x32x16_f16 v[48:63], v[156:159], v[112:115], v[48:63]
	v_add_f32_e32 v104, v94, v104
	v_add_f32_e32 v104, v95, v104
	v_cvt_pk_f16_f32 v118, v92, v93
	v_cvt_pk_f16_f32 v119, v94, v95
	s_add_i32 m0, s19, s25
	v_cmp_lt_f32_e32 vcc, s36, v104
	global_load_lds_dwordx4 v180, s[44:45]
	s_add_i32 m0, s18, s26
	s_add_u32 s44, s44, 0x2000
	global_load_lds_dwordx4 v180, s[46:47]
	s_addc_u32 s45, s45, 0
	s_add_u32 s46, s46, 0x2000
	s_addc_u32 s47, s47, 0
	s_cbranch_vccnz .Lmy_rare_2
